# context-row split-K tiles of out-projection and dense FFN down: fragment loads prefetched (rolling), LDS partial reads batched, residual base not waited early
# speedup vs baseline: 1.0078x; 1.0001x over previous
; #define LAS __attribute__((address_space(3)))
; __device__ __forceinline__ unsigned pk2(float lo, float hi) { f32x2 v = {lo, hi}; return __builtin_bit_cast(unsigned, __builtin_convertvector(v, bf2_t)); }
; __device__ __forceinline__ float bflo(unsigned u) { return __uint_as_float(u << 16); }
; __device__ __forceinline__ float bfhi(unsigned u) { return __uint_as_float(u & 0xffff0000u); }
; template <int NS  > __device__ __forceinline__ f32x4 ctx_tile(Frame& F, const bf16* A, const bf16* Bt, int r0, int c0) {
;     ...
;     for (int s = 0; s < NS; ++s) {
;         bf16x8 af[4], bf[2];
; #pragma unroll
;         for (int rt = 0; rt < 4; ++rt) af[rt] = *(const bf16x8*)(ap + (size_t)(16 * rt) * K + 32 * s);
;         bf[0] = *(const bf16x8*)(bp + 32 * s); bf[1] = *(const bf16x8*)(bp + (size_t)16 * K + 32 * s);
; #pragma unroll
;         for (int rt = 0; rt < 4; ++rt) { acc[rt][0] = __builtin_amdgcn_mfma_f32_16x16x32_bf16(bf[0], af[rt], acc[rt][0], 0, 0, 0); acc[rt][1] = __builtin_amdgcn_mfma_f32_16x16x32_bf16(bf[1], af[rt], acc[rt][1], 0, 0, 0); }
;     }
;     LAS f32x4* red = (LAS f32x4*)F.lds;
;     __syncthreads();
; #pragma unroll
;     for (int rt = 0; rt < 4; ++rt) { red[(w * 8 + 2 * rt) * 64 + lane] = acc[rt][0]; red[(w * 8 + 2 * rt + 1) * 64 + lane] = acc[rt][1]; }
;     __syncthreads();
;     const int tt = F.tid >> 6;
;     f32x4 v = red[tt * 64 + lane];
; #pragma unroll
;     for (int ww = 1; ww < 8; ++ww) v = v + red[(ww * 8 + tt) * 64 + lane];
;     return v;
; __global__ void __launch_bounds__(NWAVES * 64, 2) mk_fwd(Args args) {
;     ...
;                 bf16* hp = (bf16*)(ws + WS_H) + row * D + col; f32x4 bi;
;                 if (l == 0) bi = *(const f32x4*)(args.in[2] + F.zo + (row - ML) * D + col); else { const u32x2 hb = *(const u32x2*)hp; bi = (f32x4){bflo(hb.x), bfhi(hb.x), bflo(hb.y), bfhi(hb.y)}; }
;                 const f32x4 gv = *(const f32x4*)(g1 + 12 * D + col);
;                 const f32x4 s = ctx_tile<4>(F, (const bf16*)(ws + WS_MM), WOUT, r0, c0);
;                 const f32x4 ho = bi + gv * s; u32x2 hw; hw.x = pk2(ho[0], ho[1]); hw.y = pk2(ho[2], ho[3]); *(u32x2*)hp = hw;
.LBB13_1000:
	v_or_b32_e32 v18, s13, v30
	v_ashrrev_i32_e32 v19, 31, v18
	v_lshlrev_b64 v[18:19], 11, v[18:19]
	v_lshl_add_u64 v[22:23], v[12:13], 0, v[18:19]
	v_add_co_u32_e32 v24, vcc, s87, v22
	v_or_b32_e32 v20, s12, v30
	s_nop 0
	v_addc_co_u32_e32 v25, vcc, 0, v23, vcc
	v_add_co_u32_e32 v26, vcc, s57, v22
	v_lshlrev_b32_e32 v18, 11, v20
	s_nop 0
	v_addc_co_u32_e32 v27, vcc, 0, v23, vcc
	v_mov_b32_e32 v19, v98
	v_add_co_u32_e32 v28, vcc, s64, v22
	v_lshl_add_u64 v[18:19], v[14:15], 0, v[18:19]
	s_nop 0
	v_addc_co_u32_e32 v29, vcc, 0, v23, vcc
	v_add_co_u32_e32 v20, vcc, s87, v18
	v_readfirstlane_b32 s6, v10
	v_readfirstlane_b32 s7, v11
	v_addc_co_u32_e32 v21, vcc, 0, v19, vcc
	s_nop 3
	global_load_dwordx4 v[6:9], v8, s[6:7]
	global_load_dwordx4 v[34:37], v[22:23], off
	global_load_dwordx4 v[38:41], v[24:25], off
	global_load_dwordx4 v[42:45], v[26:27], off
	global_load_dwordx4 v[46:49], v[28:29], off
	global_load_dwordx4 v[50:53], v[18:19], off
	global_load_dwordx4 v[54:57], v[20:21], off
	global_load_dwordx4 v[58:61], v[22:23], off offset:64
	global_load_dwordx4 v[62:65], v[24:25], off offset:64
	global_load_dwordx4 v[66:69], v[26:27], off offset:64
	global_load_dwordx4 v[70:73], v[28:29], off offset:64
	global_load_dwordx4 v[74:77], v[18:19], off offset:64
	global_load_dwordx4 v[78:81], v[20:21], off offset:64
	global_load_dwordx4 v[82:85], v[22:23], off offset:128
	global_load_dwordx4 v[86:89], v[24:25], off offset:128
	global_load_dwordx4 v[90:93], v[26:27], off offset:128
	global_load_dwordx4 v[94:97], v[28:29], off offset:128
	global_load_dwordx4 v[100:103], v[18:19], off offset:128
	global_load_dwordx4 v[104:107], v[20:21], off offset:128
	global_load_dwordx4 v[108:111], v[22:23], off offset:192
	global_load_dwordx4 v[112:115], v[24:25], off offset:192
	global_load_dwordx4 v[116:119], v[26:27], off offset:192
	global_load_dwordx4 v[120:123], v[28:29], off offset:192
	global_load_dwordx4 v[124:127], v[18:19], off offset:192
	global_load_dwordx4 v[128:131], v[20:21], off offset:192
	s_waitcnt vmcnt(18)
	v_mfma_f32_16x16x32_bf16 v[166:169], v[50:53], v[34:37], 0
	v_mfma_f32_16x16x32_bf16 v[170:173], v[54:57], v[34:37], 0
	v_mfma_f32_16x16x32_bf16 v[174:177], v[50:53], v[38:41], 0
	v_mfma_f32_16x16x32_bf16 v[178:181], v[54:57], v[38:41], 0
	v_mfma_f32_16x16x32_bf16 v[182:185], v[50:53], v[42:45], 0
	v_mfma_f32_16x16x32_bf16 v[186:189], v[54:57], v[42:45], 0
	v_mfma_f32_16x16x32_bf16 v[190:193], v[50:53], v[46:49], 0
	v_mfma_f32_16x16x32_bf16 v[194:197], v[54:57], v[46:49], 0
	s_waitcnt vmcnt(12)
	v_mfma_f32_16x16x32_bf16 v[166:169], v[74:77], v[58:61], v[166:169]
	v_mfma_f32_16x16x32_bf16 v[170:173], v[78:81], v[58:61], v[170:173]
	v_mfma_f32_16x16x32_bf16 v[174:177], v[74:77], v[62:65], v[174:177]
	v_mfma_f32_16x16x32_bf16 v[178:181], v[78:81], v[62:65], v[178:181]
	v_mfma_f32_16x16x32_bf16 v[182:185], v[74:77], v[66:69], v[182:185]
	v_mfma_f32_16x16x32_bf16 v[186:189], v[78:81], v[66:69], v[186:189]
	v_mfma_f32_16x16x32_bf16 v[190:193], v[74:77], v[70:73], v[190:193]
	v_mfma_f32_16x16x32_bf16 v[194:197], v[78:81], v[70:73], v[194:197]
	s_waitcnt vmcnt(6)
	v_mfma_f32_16x16x32_bf16 v[166:169], v[100:103], v[82:85], v[166:169]
	v_mfma_f32_16x16x32_bf16 v[170:173], v[104:107], v[82:85], v[170:173]
	v_mfma_f32_16x16x32_bf16 v[174:177], v[100:103], v[86:89], v[174:177]
	v_mfma_f32_16x16x32_bf16 v[178:181], v[104:107], v[86:89], v[178:181]
	v_mfma_f32_16x16x32_bf16 v[182:185], v[100:103], v[90:93], v[182:185]
	v_mfma_f32_16x16x32_bf16 v[186:189], v[104:107], v[90:93], v[186:189]
	v_mfma_f32_16x16x32_bf16 v[190:193], v[100:103], v[94:97], v[190:193]
	v_mfma_f32_16x16x32_bf16 v[194:197], v[104:107], v[94:97], v[194:197]
	s_waitcnt vmcnt(0)
	v_mfma_f32_16x16x32_bf16 v[166:169], v[124:127], v[108:111], v[166:169]
	v_mfma_f32_16x16x32_bf16 v[170:173], v[128:131], v[108:111], v[170:173]
	v_mfma_f32_16x16x32_bf16 v[174:177], v[124:127], v[112:115], v[174:177]
	v_mfma_f32_16x16x32_bf16 v[178:181], v[128:131], v[112:115], v[178:181]
	v_mfma_f32_16x16x32_bf16 v[182:185], v[124:127], v[116:119], v[182:185]
	v_mfma_f32_16x16x32_bf16 v[186:189], v[128:131], v[116:119], v[186:189]
	v_mfma_f32_16x16x32_bf16 v[190:193], v[124:127], v[120:123], v[190:193]
	v_mfma_f32_16x16x32_bf16 v[194:197], v[128:131], v[120:123], v[194:197]
	s_barrier
	s_nop 7
	ds_write_b128 v33, v[166:169]
	ds_write_b128 v33, v[170:173] offset:1024
	ds_write_b128 v33, v[174:177] offset:2048
	ds_write_b128 v33, v[178:181] offset:3072
	ds_write_b128 v33, v[182:185] offset:4096
	ds_write_b128 v33, v[186:189] offset:5120
	ds_write_b128 v33, v[190:193] offset:6144
	ds_write_b128 v33, v[194:197] offset:7168
	s_waitcnt lgkmcnt(0)
	s_barrier
	ds_read_b128 v[100:103], v1
	ds_read_b128 v[104:107], v1 offset:8192
	ds_read_b128 v[108:111], v1 offset:16384
	ds_read_b128 v[112:115], v1 offset:24576
	ds_read_b128 v[116:119], v1 offset:32768
	ds_read_b128 v[120:123], v1 offset:40960
	ds_read_b128 v[124:127], v1 offset:49152
	ds_read_b128 v[128:131], v1 offset:57344
	s_waitcnt lgkmcnt(6)
	v_pk_add_f32 v[20:21], v[102:103], v[106:107]
	v_pk_add_f32 v[18:19], v[100:101], v[104:105]
	s_waitcnt lgkmcnt(5)
	v_pk_add_f32 v[20:21], v[20:21], v[110:111]
	v_pk_add_f32 v[18:19], v[18:19], v[108:109]
	s_waitcnt lgkmcnt(4)
	v_pk_add_f32 v[20:21], v[20:21], v[114:115]
	v_pk_add_f32 v[18:19], v[18:19], v[112:113]
	s_waitcnt lgkmcnt(3)
	v_pk_add_f32 v[20:21], v[20:21], v[118:119]
	v_pk_add_f32 v[18:19], v[18:19], v[116:117]
	s_waitcnt lgkmcnt(2)
	v_pk_add_f32 v[20:21], v[20:21], v[122:123]
	v_pk_add_f32 v[18:19], v[18:19], v[120:121]
	s_waitcnt lgkmcnt(1)
	v_pk_add_f32 v[20:21], v[20:21], v[126:127]
	v_pk_add_f32 v[18:19], v[18:19], v[124:125]
	s_waitcnt lgkmcnt(0)
	v_pk_add_f32 v[20:21], v[20:21], v[130:131]
	v_pk_add_f32 v[18:19], v[18:19], v[128:129]
	s_waitcnt vmcnt(0)
	s_and_b64 vcc, exec, s[8:9]
	s_cbranch_vccz .Loctx_f32base
	v_lshlrev_b32_e32 v2, 16, v4
	v_and_b32_e32 v3, 0xffff0000, v4
	v_lshlrev_b32_e32 v4, 16, v5
	v_and_b32_e32 v5, 0xffff0000, v5
; __device__ __forceinline__ unsigned pk2(float lo, float hi) { f32x2 v = {lo, hi}; return __builtin_bit_cast(unsigned, __builtin_convertvector(v, bf2_t)); }
; __device__ __forceinline__ float bflo(unsigned u) { return __uint_as_float(u << 16); }
; __device__ __forceinline__ float bfhi(unsigned u) { return __uint_as_float(u & 0xffff0000u); }
; __global__ void __launch_bounds__(NWAVES * 64, 2) mk_fwd(Args args) {
;     ...
;             if (!last) for (int tl = F.vcu; tl < 256; tl += F.G) {
;                 const int r0 = ML + 64 * (tl >> 5), c0 = 32 * (tl & 31);
;                 const int tt = F.tid >> 6; const size_t row = (size_t)(r0 + 16 * (tt >> 1) + (F.lane & 15)); const int col = c0 + 16 * (tt & 1) + 4 * (F.lane >> 4);
;                 bf16* hp = (bf16*)(ws + WS_H) + row * D + col; f32x4 bi;
;                 if (l == 0) bi = *(const f32x4*)(args.in[2] + F.zo + (row - ML) * D + col); else { const u32x2 hb = *(const u32x2*)hp; bi = (f32x4){bflo(hb.x), bfhi(hb.x), bflo(hb.y), bfhi(hb.y)}; }
;                 const f32x4 gv = *(const f32x4*)(g1 + 12 * D + col);
;                 const f32x4 s = ctx_tile<4>(F, (const bf16*)(ws + WS_MM), WOUT, r0, c0);
;                 const f32x4 ho = bi + gv * s; u32x2 hw; hw.x = pk2(ho[0], ho[1]); hw.y = pk2(ho[2], ho[3]); *(u32x2*)hp = hw;
.Loctx_f32base:
	v_pk_fma_f32 v[4:5], v[8:9], v[20:21], v[4:5]
	v_pk_fma_f32 v[2:3], v[6:7], v[18:19], v[2:3]
	s_nop 0
	v_cvt_pk_bf16_f32 v2, v2, v3
	v_cvt_pk_bf16_f32 v3, v4, v5
	s_add_i32 s1, s1, s0
	s_add_i32 s2, s2, s3
	s_add_i32 s10, s10, s11
	s_cmpk_lt_i32 s1, 0x100
	global_store_dwordx2 v[16:17], v[2:3], off
	s_cbranch_scc0 .LBB13_1005
.LBB13_1001:
	s_and_b32 s13, s2, 0xffffffc0
	s_addk_i32 s13, 0x4000
	v_add_u32_e32 v6, s13, v31
	s_and_b32 s12, s10, 0x3e0
	v_ashrrev_i32_e32 v7, 31, v6
	v_or_b32_e32 v8, s12, v32
	v_lshlrev_b64 v[2:3], 11, v[6:7]
	v_lshl_add_u64 v[2:3], v[156:157], 0, v[2:3]
	v_lshlrev_b32_e32 v4, 1, v8
	v_mov_b32_e32 v5, v98
	v_lshl_add_u64 v[16:17], v[2:3], 0, v[4:5]
	s_mov_b64 s[6:7], -1
	s_and_b64 vcc, exec, s[8:9]
	s_cbranch_vccz .LBB13_1003
	global_load_dwordx2 v[4:5], v[16:17], off
	s_mov_b64 s[6:7], 0
.LBB13_1003:
	s_andn2_b64 vcc, exec, s[6:7]
	v_lshlrev_b32_e32 v8, 2, v8
	s_cbranch_vccnz .LBB13_1000
	v_lshlrev_b64 v[2:3], 12, v[6:7]
	v_lshl_add_u64 v[2:3], s[4:5], 0, v[2:3]
	v_mov_b32_e32 v9, v98
	v_lshl_add_u64 v[2:3], v[2:3], 0, v[8:9]
	v_add_co_u32_e32 v2, vcc, 0xfc000000, v2
	s_nop 1
	v_addc_co_u32_e32 v3, vcc, -1, v3, vcc
	global_load_dwordx4 v[2:5], v[2:3], off
	s_branch .LBB13_1000

; template <int NS  > __device__ __forceinline__ f32x4 ctx_tile(Frame& F, const bf16* A, const bf16* Bt, int r0, int c0) {
;     ...
;     const bf16* ap = A + (size_t)(r0 + l15) * K + w * (K / 8) + 8 * g;
;     const bf16* bp = Bt + (size_t)(c0 + l15) * K + w * (K / 8) + 8 * g;
;     f32x4 acc[4][2];
; #pragma unroll
;     for (int rt = 0; rt < 4; ++rt) { acc[rt][0] = (f32x4){0.f, 0.f, 0.f, 0.f}; acc[rt][1] = (f32x4){0.f, 0.f, 0.f, 0.f}; }
; #pragma unroll 4
;     for (int s = 0; s < NS; ++s) {
;         bf16x8 af[4], bf[2];
; #pragma unroll
;         for (int rt = 0; rt < 4; ++rt) af[rt] = *(const bf16x8*)(ap + (size_t)(16 * rt) * K + 32 * s);
;         bf[0] = *(const bf16x8*)(bp + 32 * s); bf[1] = *(const bf16x8*)(bp + (size_t)16 * K + 32 * s);
; #pragma unroll
;         for (int rt = 0; rt < 4; ++rt) { acc[rt][0] = __builtin_amdgcn_mfma_f32_16x16x32_bf16(bf[0], af[rt], acc[rt][0], 0, 0, 0); acc[rt][1] = __builtin_amdgcn_mfma_f32_16x16x32_bf16(bf[1], af[rt], acc[rt][1], 0, 0, 0); }
;     }
; __global__ void __launch_bounds__(NWAVES * 64, 2) mk_fwd(Args args) {
;     ...
;                 for (int tl = F.vcu; tl < 256; tl += F.G) {
;                     const int r0 = ML + 64 * (tl >> 5), c0 = 32 * (tl & 31);
;                     const int tt = F.tid >> 6; const size_t row = (size_t)(r0 + 16 * (tt >> 1) + (F.lane & 15)); const int col = c0 + 16 * (tt & 1) + 4 * (F.lane >> 4);
;                     bf16* hp = (bf16*)(ws + WS_H) + row * D + col; const u32x2 hb = *(const u32x2*)hp; const f32x4 gv = *(const f32x4*)(g2 + 12 * D + col);
;                     const f32x4 s = ctx_tile<11>(F, (const bf16*)(ws + WS_HID), WD, r0, c0);
.LBB13_1547:
	s_and_b32 s11, s2, 0xffffffc0
	s_addk_i32 s11, 0x4000
	v_add_u32_e32 v2, s11, v67
	s_and_b32 s12, s6, 0x3e0
	v_ashrrev_i32_e32 v3, 31, v2
	v_or_b32_e32 v6, s12, v68
	v_lshlrev_b64 v[2:3], 11, v[2:3]
	v_lshl_add_u64 v[2:3], s[8:9], 0, v[2:3]
	v_lshlrev_b32_e32 v4, 1, v6
	v_mov_b32_e32 v5, v98
	v_lshl_add_u64 v[58:59], v[2:3], 0, v[4:5]
	v_lshlrev_b32_e32 v2, 2, v6
	v_or_b32_e32 v6, s11, v66
	v_or_b32_e32 v7, s12, v66
	v_mad_i64_i32 v[38:39], s[12:13], v6, s89, v[54:55]
	v_add_co_u32_e32 v40, vcc, s88, v38
	s_mov_b32 s11, 0x2c000
	s_nop 0
	v_addc_co_u32_e32 v41, vcc, 0, v39, vcc
	v_add_co_u32_e32 v42, vcc, s11, v38
	v_mul_u32_u24_e32 v7, 0xb00, v7
	s_nop 0
	v_addc_co_u32_e32 v43, vcc, 0, v39, vcc
	s_mov_b32 s11, 0x42000
	v_lshlrev_b32_e32 v6, 1, v7
	v_mov_b32_e32 v7, v98
	v_add_co_u32_e32 v44, vcc, s11, v38
	v_lshl_add_u64 v[62:63], v[56:57], 0, v[6:7]
	s_nop 0
	v_addc_co_u32_e32 v45, vcc, 0, v39, vcc
	v_add_co_u32_e32 v64, vcc, s88, v62
	global_load_dwordx2 v[60:61], v[58:59], off
	s_nop 0
	v_addc_co_u32_e32 v65, vcc, 0, v63, vcc
	global_load_dwordx4 v[2:5], v2, s[4:5]
	global_load_dwordx4 v[72:75], v[38:39], off
	global_load_dwordx4 v[76:79], v[40:41], off
	global_load_dwordx4 v[80:83], v[42:43], off
	global_load_dwordx4 v[84:87], v[44:45], off
	global_load_dwordx4 v[88:91], v[62:63], off
	global_load_dwordx4 v[92:95], v[64:65], off
	global_load_dwordx4 v[100:103], v[38:39], off offset:64
	global_load_dwordx4 v[104:107], v[40:41], off offset:64
	global_load_dwordx4 v[108:111], v[42:43], off offset:64
	global_load_dwordx4 v[112:115], v[44:45], off offset:64
	global_load_dwordx4 v[116:119], v[62:63], off offset:64
	global_load_dwordx4 v[120:123], v[64:65], off offset:64
	global_load_dwordx4 v[124:127], v[38:39], off offset:128
	global_load_dwordx4 v[128:131], v[40:41], off offset:128
	global_load_dwordx4 v[132:135], v[42:43], off offset:128
	global_load_dwordx4 v[136:139], v[44:45], off offset:128
	global_load_dwordx4 v[140:143], v[62:63], off offset:128
	global_load_dwordx4 v[144:147], v[64:65], off offset:128
	global_load_dwordx4 v[148:151], v[38:39], off offset:192
	global_load_dwordx4 v[152:155], v[40:41], off offset:192
	global_load_dwordx4 v[156:159], v[42:43], off offset:192
	global_load_dwordx4 v[160:163], v[44:45], off offset:192
	global_load_dwordx4 v[164:167], v[62:63], off offset:192
	global_load_dwordx4 v[168:171], v[64:65], off offset:192
	global_load_dwordx4 v[172:175], v[38:39], off offset:256
	global_load_dwordx4 v[176:179], v[40:41], off offset:256
	global_load_dwordx4 v[180:183], v[42:43], off offset:256
	global_load_dwordx4 v[184:187], v[44:45], off offset:256
	global_load_dwordx4 v[188:191], v[62:63], off offset:256
	global_load_dwordx4 v[192:195], v[64:65], off offset:256
	global_load_dwordx4 v[208:211], v[38:39], off offset:320
	global_load_dwordx4 v[212:215], v[40:41], off offset:320
	global_load_dwordx4 v[216:219], v[42:43], off offset:320
	global_load_dwordx4 v[220:223], v[44:45], off offset:320
	global_load_dwordx4 v[224:227], v[62:63], off offset:320
	global_load_dwordx4 v[228:231], v[64:65], off offset:320
	s_waitcnt vmcnt(30)
	v_mfma_f32_16x16x32_bf16 v[6:9], v[88:91], v[72:75], 0
	v_mfma_f32_16x16x32_bf16 v[10:13], v[92:95], v[72:75], 0
	v_mfma_f32_16x16x32_bf16 v[14:17], v[88:91], v[76:79], 0
	v_mfma_f32_16x16x32_bf16 v[18:21], v[92:95], v[76:79], 0
	v_mfma_f32_16x16x32_bf16 v[22:25], v[88:91], v[80:83], 0
	v_mfma_f32_16x16x32_bf16 v[26:29], v[92:95], v[80:83], 0
	v_mfma_f32_16x16x32_bf16 v[30:33], v[88:91], v[84:87], 0
	v_mfma_f32_16x16x32_bf16 v[34:37], v[92:95], v[84:87], 0
	global_load_dwordx4 v[72:75], v[38:39], off offset:384
	global_load_dwordx4 v[76:79], v[40:41], off offset:384
	global_load_dwordx4 v[80:83], v[42:43], off offset:384
	global_load_dwordx4 v[84:87], v[44:45], off offset:384
	global_load_dwordx4 v[88:91], v[62:63], off offset:384
	global_load_dwordx4 v[92:95], v[64:65], off offset:384
	s_waitcnt vmcnt(30)
	v_mfma_f32_16x16x32_bf16 v[6:9], v[116:119], v[100:103], v[6:9]
	v_mfma_f32_16x16x32_bf16 v[10:13], v[120:123], v[100:103], v[10:13]
	v_mfma_f32_16x16x32_bf16 v[14:17], v[116:119], v[104:107], v[14:17]
	v_mfma_f32_16x16x32_bf16 v[18:21], v[120:123], v[104:107], v[18:21]
	v_mfma_f32_16x16x32_bf16 v[22:25], v[116:119], v[108:111], v[22:25]
	v_mfma_f32_16x16x32_bf16 v[26:29], v[120:123], v[108:111], v[26:29]
	v_mfma_f32_16x16x32_bf16 v[30:33], v[116:119], v[112:115], v[30:33]
	v_mfma_f32_16x16x32_bf16 v[34:37], v[120:123], v[112:115], v[34:37]
	global_load_dwordx4 v[100:103], v[38:39], off offset:448
	global_load_dwordx4 v[104:107], v[40:41], off offset:448
	global_load_dwordx4 v[108:111], v[42:43], off offset:448
	global_load_dwordx4 v[112:115], v[44:45], off offset:448
	global_load_dwordx4 v[116:119], v[62:63], off offset:448
	global_load_dwordx4 v[120:123], v[64:65], off offset:448
	s_waitcnt vmcnt(30)
	v_mfma_f32_16x16x32_bf16 v[6:9], v[140:143], v[124:127], v[6:9]
	v_mfma_f32_16x16x32_bf16 v[10:13], v[144:147], v[124:127], v[10:13]
	v_mfma_f32_16x16x32_bf16 v[14:17], v[140:143], v[128:131], v[14:17]
	v_mfma_f32_16x16x32_bf16 v[18:21], v[144:147], v[128:131], v[18:21]
	v_mfma_f32_16x16x32_bf16 v[22:25], v[140:143], v[132:135], v[22:25]
	v_mfma_f32_16x16x32_bf16 v[26:29], v[144:147], v[132:135], v[26:29]
	v_mfma_f32_16x16x32_bf16 v[30:33], v[140:143], v[136:139], v[30:33]
	v_mfma_f32_16x16x32_bf16 v[34:37], v[144:147], v[136:139], v[34:37]
	global_load_dwordx4 v[124:127], v[38:39], off offset:512
	global_load_dwordx4 v[128:131], v[40:41], off offset:512
	global_load_dwordx4 v[132:135], v[42:43], off offset:512
	global_load_dwordx4 v[136:139], v[44:45], off offset:512
	global_load_dwordx4 v[140:143], v[62:63], off offset:512
	global_load_dwordx4 v[144:147], v[64:65], off offset:512
	s_waitcnt vmcnt(30)
; template <int NS  > __device__ __forceinline__ f32x4 ctx_tile(Frame& F, const bf16* A, const bf16* Bt, int r0, int c0) {
;     ...
;     for (int s = 0; s < NS; ++s) {
;         bf16x8 af[4], bf[2];
; #pragma unroll
;         for (int rt = 0; rt < 4; ++rt) af[rt] = *(const bf16x8*)(ap + (size_t)(16 * rt) * K + 32 * s);
;         bf[0] = *(const bf16x8*)(bp + 32 * s); bf[1] = *(const bf16x8*)(bp + (size_t)16 * K + 32 * s);
; #pragma unroll
;         for (int rt = 0; rt < 4; ++rt) { acc[rt][0] = __builtin_amdgcn_mfma_f32_16x16x32_bf16(bf[0], af[rt], acc[rt][0], 0, 0, 0); acc[rt][1] = __builtin_amdgcn_mfma_f32_16x16x32_bf16(bf[1], af[rt], acc[rt][1], 0, 0, 0); }
;     }
	v_mfma_f32_16x16x32_bf16 v[6:9], v[164:167], v[148:151], v[6:9]
	v_mfma_f32_16x16x32_bf16 v[10:13], v[168:171], v[148:151], v[10:13]
	v_mfma_f32_16x16x32_bf16 v[14:17], v[164:167], v[152:155], v[14:17]
	v_mfma_f32_16x16x32_bf16 v[18:21], v[168:171], v[152:155], v[18:21]
	v_mfma_f32_16x16x32_bf16 v[22:25], v[164:167], v[156:159], v[22:25]
	v_mfma_f32_16x16x32_bf16 v[26:29], v[168:171], v[156:159], v[26:29]
	v_mfma_f32_16x16x32_bf16 v[30:33], v[164:167], v[160:163], v[30:33]
	v_mfma_f32_16x16x32_bf16 v[34:37], v[168:171], v[160:163], v[34:37]
	global_load_dwordx4 v[148:151], v[38:39], off offset:576
	global_load_dwordx4 v[152:155], v[40:41], off offset:576
	global_load_dwordx4 v[156:159], v[42:43], off offset:576
	global_load_dwordx4 v[160:163], v[44:45], off offset:576
	global_load_dwordx4 v[164:167], v[62:63], off offset:576
	global_load_dwordx4 v[168:171], v[64:65], off offset:576
	s_waitcnt vmcnt(30)
	v_mfma_f32_16x16x32_bf16 v[6:9], v[188:191], v[172:175], v[6:9]
	v_mfma_f32_16x16x32_bf16 v[10:13], v[192:195], v[172:175], v[10:13]
	v_mfma_f32_16x16x32_bf16 v[14:17], v[188:191], v[176:179], v[14:17]
	v_mfma_f32_16x16x32_bf16 v[18:21], v[192:195], v[176:179], v[18:21]
	v_mfma_f32_16x16x32_bf16 v[22:25], v[188:191], v[180:183], v[22:25]
	v_mfma_f32_16x16x32_bf16 v[26:29], v[192:195], v[180:183], v[26:29]
	v_mfma_f32_16x16x32_bf16 v[30:33], v[188:191], v[184:187], v[30:33]
	v_mfma_f32_16x16x32_bf16 v[34:37], v[192:195], v[184:187], v[34:37]
	global_load_dwordx4 v[172:175], v[38:39], off offset:640
	global_load_dwordx4 v[176:179], v[40:41], off offset:640
	global_load_dwordx4 v[180:183], v[42:43], off offset:640
	global_load_dwordx4 v[184:187], v[44:45], off offset:640
	global_load_dwordx4 v[188:191], v[62:63], off offset:640
	global_load_dwordx4 v[192:195], v[64:65], off offset:640
	s_waitcnt vmcnt(30)
	v_mfma_f32_16x16x32_bf16 v[6:9], v[224:227], v[208:211], v[6:9]
	v_mfma_f32_16x16x32_bf16 v[10:13], v[228:231], v[208:211], v[10:13]
	v_mfma_f32_16x16x32_bf16 v[14:17], v[224:227], v[212:215], v[14:17]
	v_mfma_f32_16x16x32_bf16 v[18:21], v[228:231], v[212:215], v[18:21]
	v_mfma_f32_16x16x32_bf16 v[22:25], v[224:227], v[216:219], v[22:25]
	v_mfma_f32_16x16x32_bf16 v[26:29], v[228:231], v[216:219], v[26:29]
	v_mfma_f32_16x16x32_bf16 v[30:33], v[224:227], v[220:223], v[30:33]
	v_mfma_f32_16x16x32_bf16 v[34:37], v[228:231], v[220:223], v[34:37]
	s_waitcnt vmcnt(24)
	v_mfma_f32_16x16x32_bf16 v[6:9], v[88:91], v[72:75], v[6:9]
	v_mfma_f32_16x16x32_bf16 v[10:13], v[92:95], v[72:75], v[10:13]
	v_mfma_f32_16x16x32_bf16 v[14:17], v[88:91], v[76:79], v[14:17]
	v_mfma_f32_16x16x32_bf16 v[18:21], v[92:95], v[76:79], v[18:21]
	v_mfma_f32_16x16x32_bf16 v[22:25], v[88:91], v[80:83], v[22:25]
	v_mfma_f32_16x16x32_bf16 v[26:29], v[92:95], v[80:83], v[26:29]
	v_mfma_f32_16x16x32_bf16 v[30:33], v[88:91], v[84:87], v[30:33]
	v_mfma_f32_16x16x32_bf16 v[34:37], v[92:95], v[84:87], v[34:37]
	s_waitcnt vmcnt(18)
	v_mfma_f32_16x16x32_bf16 v[6:9], v[116:119], v[100:103], v[6:9]
	v_mfma_f32_16x16x32_bf16 v[10:13], v[120:123], v[100:103], v[10:13]
	v_mfma_f32_16x16x32_bf16 v[14:17], v[116:119], v[104:107], v[14:17]
	v_mfma_f32_16x16x32_bf16 v[18:21], v[120:123], v[104:107], v[18:21]
	v_mfma_f32_16x16x32_bf16 v[22:25], v[116:119], v[108:111], v[22:25]
	v_mfma_f32_16x16x32_bf16 v[26:29], v[120:123], v[108:111], v[26:29]
	v_mfma_f32_16x16x32_bf16 v[30:33], v[116:119], v[112:115], v[30:33]
	v_mfma_f32_16x16x32_bf16 v[34:37], v[120:123], v[112:115], v[34:37]
	s_waitcnt vmcnt(12)
	v_mfma_f32_16x16x32_bf16 v[6:9], v[140:143], v[124:127], v[6:9]
	v_mfma_f32_16x16x32_bf16 v[10:13], v[144:147], v[124:127], v[10:13]
	v_mfma_f32_16x16x32_bf16 v[14:17], v[140:143], v[128:131], v[14:17]
	v_mfma_f32_16x16x32_bf16 v[18:21], v[144:147], v[128:131], v[18:21]
	v_mfma_f32_16x16x32_bf16 v[22:25], v[140:143], v[132:135], v[22:25]
	v_mfma_f32_16x16x32_bf16 v[26:29], v[144:147], v[132:135], v[26:29]
	v_mfma_f32_16x16x32_bf16 v[30:33], v[140:143], v[136:139], v[30:33]
	v_mfma_f32_16x16x32_bf16 v[34:37], v[144:147], v[136:139], v[34:37]
	s_waitcnt vmcnt(6)
	v_mfma_f32_16x16x32_bf16 v[6:9], v[164:167], v[148:151], v[6:9]
	v_mfma_f32_16x16x32_bf16 v[10:13], v[168:171], v[148:151], v[10:13]
	v_mfma_f32_16x16x32_bf16 v[14:17], v[164:167], v[152:155], v[14:17]
	v_mfma_f32_16x16x32_bf16 v[18:21], v[168:171], v[152:155], v[18:21]
	v_mfma_f32_16x16x32_bf16 v[22:25], v[164:167], v[156:159], v[22:25]
	v_mfma_f32_16x16x32_bf16 v[26:29], v[168:171], v[156:159], v[26:29]
	v_mfma_f32_16x16x32_bf16 v[30:33], v[164:167], v[160:163], v[30:33]
	v_mfma_f32_16x16x32_bf16 v[34:37], v[168:171], v[160:163], v[34:37]
	s_waitcnt vmcnt(0)
	v_mfma_f32_16x16x32_bf16 v[6:9], v[188:191], v[172:175], v[6:9]
	v_mfma_f32_16x16x32_bf16 v[10:13], v[192:195], v[172:175], v[10:13]
	v_mfma_f32_16x16x32_bf16 v[14:17], v[188:191], v[176:179], v[14:17]
	v_mfma_f32_16x16x32_bf16 v[18:21], v[192:195], v[176:179], v[18:21]
	v_mfma_f32_16x16x32_bf16 v[22:25], v[188:191], v[180:183], v[22:25]
	v_mfma_f32_16x16x32_bf16 v[26:29], v[192:195], v[180:183], v[26:29]
	v_mfma_f32_16x16x32_bf16 v[30:33], v[188:191], v[184:187], v[30:33]
	v_mfma_f32_16x16x32_bf16 v[34:37], v[192:195], v[184:187], v[34:37]
	s_barrier
; #define LAS __attribute__((address_space(3)))
; __device__ __forceinline__ unsigned pk2(float lo, float hi) { f32x2 v = {lo, hi}; return __builtin_bit_cast(unsigned, __builtin_convertvector(v, bf2_t)); }
; __device__ __forceinline__ float bflo(unsigned u) { return __uint_as_float(u << 16); }
; __device__ __forceinline__ float bfhi(unsigned u) { return __uint_as_float(u & 0xffff0000u); }
; template <int NS  > __device__ __forceinline__ f32x4 ctx_tile(Frame& F, const bf16* A, const bf16* Bt, int r0, int c0) {
;     ...
;     LAS f32x4* red = (LAS f32x4*)F.lds;
;     __syncthreads();
; #pragma unroll
;     for (int rt = 0; rt < 4; ++rt) { red[(w * 8 + 2 * rt) * 64 + lane] = acc[rt][0]; red[(w * 8 + 2 * rt + 1) * 64 + lane] = acc[rt][1]; }
;     __syncthreads();
;     const int tt = F.tid >> 6;
;     f32x4 v = red[tt * 64 + lane];
; #pragma unroll
;     for (int ww = 1; ww < 8; ++ww) v = v + red[(ww * 8 + tt) * 64 + lane];
;     return v;
; __global__ void __launch_bounds__(NWAVES * 64, 2) mk_fwd(Args args) {
;     ...
;                     bf16* hp = (bf16*)(ws + WS_H) + row * D + col; const u32x2 hb = *(const u32x2*)hp; const f32x4 gv = *(const f32x4*)(g2 + 12 * D + col);
;                     const f32x4 s = ctx_tile<11>(F, (const bf16*)(ws + WS_HID), WD, r0, c0);
;                     const f32x4 ho = (f32x4){bflo(hb.x), bfhi(hb.x), bflo(hb.y), bfhi(hb.y)} + gv * s; u32x2 hw; hw.x = pk2(ho[0], ho[1]); hw.y = pk2(ho[2], ho[3]); *(u32x2*)hp = hw;
	s_nop 7
	ds_write_b128 v69, v[6:9]
	ds_write_b128 v69, v[10:13] offset:1024
	ds_write_b128 v69, v[14:17] offset:2048
	ds_write_b128 v69, v[18:21] offset:3072
	ds_write_b128 v69, v[22:25] offset:4096
	ds_write_b128 v69, v[26:29] offset:5120
	ds_write_b128 v69, v[30:33] offset:6144
	ds_write_b128 v69, v[34:37] offset:7168
	s_waitcnt lgkmcnt(0)
	s_barrier
	ds_read_b128 v[100:103], v70
	ds_read_b128 v[104:107], v70 offset:8192
	ds_read_b128 v[108:111], v70 offset:16384
	ds_read_b128 v[112:115], v70 offset:24576
	ds_read_b128 v[116:119], v70 offset:32768
	ds_read_b128 v[120:123], v70 offset:40960
	ds_read_b128 v[124:127], v70 offset:49152
	ds_read_b128 v[128:131], v70 offset:57344
	s_waitcnt lgkmcnt(6)
	v_pk_add_f32 v[48:49], v[102:103], v[106:107]
	v_pk_add_f32 v[46:47], v[100:101], v[104:105]
	s_waitcnt lgkmcnt(5)
	v_pk_add_f32 v[48:49], v[48:49], v[110:111]
	v_pk_add_f32 v[46:47], v[46:47], v[108:109]
	s_waitcnt lgkmcnt(4)
	v_pk_add_f32 v[48:49], v[48:49], v[114:115]
	v_pk_add_f32 v[46:47], v[46:47], v[112:113]
	s_waitcnt lgkmcnt(3)
	v_pk_add_f32 v[48:49], v[48:49], v[118:119]
	v_pk_add_f32 v[46:47], v[46:47], v[116:117]
	s_waitcnt lgkmcnt(2)
	v_pk_add_f32 v[48:49], v[48:49], v[122:123]
	v_pk_add_f32 v[46:47], v[46:47], v[120:121]
	s_waitcnt lgkmcnt(1)
	v_pk_add_f32 v[48:49], v[48:49], v[126:127]
	v_pk_add_f32 v[46:47], v[46:47], v[124:125]
	s_waitcnt lgkmcnt(0)
	v_pk_add_f32 v[48:49], v[48:49], v[130:131]
	v_pk_add_f32 v[46:47], v[46:47], v[128:129]
	s_waitcnt vmcnt(0)
	v_lshlrev_b32_e32 v50, 16, v60
	v_and_b32_e32 v51, 0xffff0000, v60
	v_lshlrev_b32_e32 v52, 16, v61
	v_and_b32_e32 v53, 0xffff0000, v61
	v_pk_fma_f32 v[4:5], v[4:5], v[48:49], v[52:53]
	v_pk_fma_f32 v[2:3], v[2:3], v[46:47], v[50:51]
	s_nop 0
	v_cvt_pk_bf16_f32 v2, v2, v3
	v_cvt_pk_bf16_f32 v3, v4, v5
	s_add_i32 s10, s10, s28
	s_add_i32 s2, s2, s3
	s_add_i32 s6, s6, s7
	s_cmpk_gt_i32 s10, 0xff
	global_store_dwordx2 v[58:59], v[2:3], off
	s_cbranch_scc0 .LBB13_1547
